# v24 = v20 with the RWKV-scan conversion stores at default cache policy (no nt), so the paired 64-byte halves merge in L2
# speedup vs baseline: 1.0092x; 1.0092x over previous
.LBB0_656:
	s_lshl_b32 s62, s65, 6
	s_sub_i32 s61, s96, s62
	s_and_b64 s[58:59], s[58:59], exec
	s_cselect_b32 s63, 64, s61
	s_lshl_b32 s58, s75, 3
	s_add_i32 s58, s58, 0
	s_add_i32 s58, s58, 0x20040
	v_mov_b32_e32 v90, s58
	s_mul_i32 s72, s56, s96
	ds_read_b64 v[90:91], v90
	s_lshl_b64 s[58:59], s[72:73], s60
	s_lshl_b32 s60, s64, 5
	s_mul_i32 s59, s59, s74
	s_mul_hi_u32 s64, s58, s74
	s_add_i32 s59, s64, s59
	s_mul_i32 s58, s58, s74
	s_lshl_b64 s[58:59], s[58:59], 1
	s_waitcnt lgkmcnt(0)
	v_lshl_add_u64 v[90:91], v[90:91], 0, s[58:59]
	s_ashr_i32 s58, s62, 31
	s_mul_i32 s58, s56, s58
	s_mul_hi_u32 s59, s56, s62
	s_add_i32 s58, s59, s58
	s_mul_i32 s59, s57, s62
	s_add_i32 s59, s58, s59
	s_mul_i32 s58, s56, s62
	s_ashr_i32 s61, s60, 31
	s_lshl_b64 s[58:59], s[58:59], 1
	v_lshl_add_u64 v[90:91], v[90:91], 0, s[58:59]
	s_lshl_b64 s[58:59], s[60:61], 1
	v_mul_u32_u24_e32 v92, s56, v130
	v_lshl_add_u64 v[90:91], v[90:91], 0, s[58:59]
	v_lshlrev_b32_e32 v132, 1, v92
	v_lshl_add_u64 v[90:91], v[90:91], 0, v[132:133]
	v_lshlrev_b32_e32 v132, 1, v140
	v_cvt_pk_bf16_f32 v58, v58, v62
	v_cvt_pk_bf16_f32 v62, v66, v70
	v_cvt_pk_bf16_f32 v66, v74, v78
	v_cvt_pk_bf16_f32 v70, v82, v86
	v_cmp_gt_i32_e32 vcc, s63, v130
	v_lshl_add_u64 v[94:95], v[90:91], 0, v[132:133]
	s_lshl_b64 s[56:57], s[56:57], 1
	v_cndmask_b32_e32 v93, 0, v70, vcc
	v_cndmask_b32_e32 v92, 0, v66, vcc
	v_cndmask_b32_e32 v91, 0, v62, vcc
	v_cndmask_b32_e32 v90, 0, v58, vcc
	v_cvt_pk_bf16_f32 v58, v59, v63
	v_cvt_pk_bf16_f32 v59, v67, v71
	v_cvt_pk_bf16_f32 v62, v75, v79
	v_cvt_pk_bf16_f32 v63, v83, v87
	global_store_dwordx4 v[94:95], v[90:93], off
	v_cvt_pk_bf16_f32 v60, v60, v64
	v_cvt_pk_bf16_f32 v64, v84, v88
	v_cndmask_b32_e32 v93, 0, v63, vcc
	v_cndmask_b32_e32 v92, 0, v62, vcc
	v_cndmask_b32_e32 v91, 0, v59, vcc
	v_cndmask_b32_e32 v90, 0, v58, vcc
	v_lshl_add_u64 v[58:59], v[94:95], 0, s[56:57]
	v_cvt_pk_bf16_f32 v62, v68, v72
	v_cvt_pk_bf16_f32 v63, v76, v80
	s_add_i32 s65, s80, s33
	global_store_dwordx4 v[58:59], v[90:93], off
	s_min_i32 s72, s65, 0x324ff
	s_cmpk_gt_i32 s65, 0x19ff
	v_cndmask_b32_e32 v93, 0, v64, vcc
	v_cndmask_b32_e32 v92, 0, v63, vcc
	v_cndmask_b32_e32 v91, 0, v62, vcc
	v_cndmask_b32_e32 v90, 0, v60, vcc
	v_lshl_add_u64 v[62:63], v[58:59], 0, s[56:57]
	v_cvt_pk_bf16_f32 v58, v61, v65
	v_cvt_pk_bf16_f32 v59, v69, v73
	v_cvt_pk_bf16_f32 v60, v77, v81
	v_cvt_pk_bf16_f32 v61, v85, v89
	global_store_dwordx4 v[62:63], v[90:93], off
	v_cndmask_b32_e32 v61, 0, v61, vcc
	v_cndmask_b32_e32 v60, 0, v60, vcc
	v_cndmask_b32_e32 v59, 0, v59, vcc
	v_cndmask_b32_e32 v58, 0, v58, vcc
	v_lshl_add_u64 v[62:63], v[62:63], 0, s[56:57]
	s_mov_b64 s[96:97], -1
	global_store_dwordx4 v[62:63], v[58:61], off
	s_cbranch_scc0 .LBB0_681
	s_cmpk_gt_u32 s65, 0x21ff
	s_cbranch_scc0 .LBB0_678
	s_cmpk_gt_u32 s65, 0x4dff
	s_cbranch_scc0 .LBB0_675
	s_cmpk_gt_u32 s65, 0x63ff
	s_cbranch_scc0 .LBB0_672
	s_mov_b64 s[58:59], -1
	s_cmpk_gt_u32 s65, 0x7cff
	s_cbranch_scc0 .LBB0_669
	s_cmpk_gt_u32 s65, 0x84ff
	s_cbranch_scc0 .LBB0_666
	s_mov_b64 s[60:61], -1
	s_cmp_gt_u32 s65, 0x244ff
	s_mov_b64 s[56:57], -1
	s_cbranch_scc0 .LBB0_664
	s_add_i32 s56, s72, 0xbb00
	s_bfe_u32 s57, s56, 0x6000a
	s_mulk_i32 s57, 0x2493
	s_lshr_b32 s64, s57, 16
	s_mul_i32 s57, s64, 0x1c00
	s_sub_i32 s56, s56, s57
	s_bfe_u32 s75, s56, 0x50001
	s_bfe_u32 s74, s56, 0xa0006
	s_lshl_b32 s74, s74, 1
	s_and_b32 s56, s56, 1
	s_or_b32 s74, s74, s56
	s_mov_b64 s[56:57], 0

.LBB0_715:
	s_lshl_b32 s62, s65, 6
	s_sub_i32 s61, s96, s62
	s_and_b64 s[58:59], s[58:59], exec
	s_cselect_b32 s63, 64, s61
	s_lshl_b32 s58, s75, 3
	s_add_i32 s58, s58, 0
	s_add_i32 s58, s58, 0x20040
	v_mov_b32_e32 v90, s58
	s_mul_i32 s72, s56, s96
	ds_read_b64 v[90:91], v90
	s_lshl_b64 s[58:59], s[72:73], s60
	s_lshl_b32 s60, s64, 5
	s_mul_i32 s59, s59, s74
	s_mul_hi_u32 s64, s58, s74
	s_add_i32 s59, s64, s59
	s_mul_i32 s58, s58, s74
	s_lshl_b64 s[58:59], s[58:59], 1
	s_waitcnt lgkmcnt(0)
	v_lshl_add_u64 v[90:91], v[90:91], 0, s[58:59]
	s_ashr_i32 s58, s62, 31
	s_mul_i32 s58, s56, s58
	s_mul_hi_u32 s59, s56, s62
	s_add_i32 s58, s59, s58
	s_mul_i32 s59, s57, s62
	s_add_i32 s59, s58, s59
	s_mul_i32 s58, s56, s62
	s_ashr_i32 s61, s60, 31
	s_lshl_b64 s[58:59], s[58:59], 1
	v_lshl_add_u64 v[90:91], v[90:91], 0, s[58:59]
	s_lshl_b64 s[58:59], s[60:61], 1
	v_mul_u32_u24_e32 v92, s56, v130
	v_lshl_add_u64 v[90:91], v[90:91], 0, s[58:59]
	v_lshlrev_b32_e32 v132, 1, v92
	v_lshl_add_u64 v[90:91], v[90:91], 0, v[132:133]
	v_lshlrev_b32_e32 v132, 1, v140
	v_cvt_pk_bf16_f32 v58, v58, v62
	v_cvt_pk_bf16_f32 v62, v66, v70
	v_cvt_pk_bf16_f32 v66, v74, v78
	v_cvt_pk_bf16_f32 v70, v82, v86
	v_cmp_gt_i32_e32 vcc, s63, v130
	v_lshl_add_u64 v[94:95], v[90:91], 0, v[132:133]
	s_lshl_b64 s[56:57], s[56:57], 1
	v_cndmask_b32_e32 v93, 0, v70, vcc
	v_cndmask_b32_e32 v92, 0, v66, vcc
	v_cndmask_b32_e32 v91, 0, v62, vcc
	v_cndmask_b32_e32 v90, 0, v58, vcc
	v_cvt_pk_bf16_f32 v58, v59, v63
	v_cvt_pk_bf16_f32 v59, v67, v71
	v_cvt_pk_bf16_f32 v62, v75, v79
	v_cvt_pk_bf16_f32 v63, v83, v87
	global_store_dwordx4 v[94:95], v[90:93], off
	v_cvt_pk_bf16_f32 v60, v60, v64
	v_cvt_pk_bf16_f32 v64, v84, v88
	v_cndmask_b32_e32 v93, 0, v63, vcc
	v_cndmask_b32_e32 v92, 0, v62, vcc
	v_cndmask_b32_e32 v91, 0, v59, vcc
	v_cndmask_b32_e32 v90, 0, v58, vcc
	v_lshl_add_u64 v[58:59], v[94:95], 0, s[56:57]
	v_cvt_pk_bf16_f32 v62, v68, v72
	v_cvt_pk_bf16_f32 v63, v76, v80
	s_add_i32 s33, s88, s33
	global_store_dwordx4 v[58:59], v[90:93], off
	s_min_i32 s72, s33, 0x324ff
	s_cmpk_gt_i32 s33, 0x19ff
	v_cndmask_b32_e32 v93, 0, v64, vcc
	v_cndmask_b32_e32 v92, 0, v63, vcc
	v_cndmask_b32_e32 v91, 0, v62, vcc
	v_cndmask_b32_e32 v90, 0, v60, vcc
	v_lshl_add_u64 v[62:63], v[58:59], 0, s[56:57]
	v_cvt_pk_bf16_f32 v58, v61, v65
	v_cvt_pk_bf16_f32 v59, v69, v73
	v_cvt_pk_bf16_f32 v60, v77, v81
	v_cvt_pk_bf16_f32 v61, v85, v89
	global_store_dwordx4 v[62:63], v[90:93], off
	v_cndmask_b32_e32 v61, 0, v61, vcc
	v_cndmask_b32_e32 v60, 0, v60, vcc
	v_cndmask_b32_e32 v59, 0, v59, vcc
	v_cndmask_b32_e32 v58, 0, v58, vcc
	v_lshl_add_u64 v[62:63], v[62:63], 0, s[56:57]
	s_mov_b64 s[96:97], -1
	global_store_dwordx4 v[62:63], v[58:61], off
	s_cbranch_scc0 .LBB0_740
	s_cmpk_gt_u32 s33, 0x21ff
	s_cbranch_scc0 .LBB0_737
	s_cmpk_gt_u32 s33, 0x4dff
	s_cbranch_scc0 .LBB0_734
	s_cmpk_gt_u32 s33, 0x63ff
	s_cbranch_scc0 .LBB0_731
	s_mov_b64 s[58:59], -1
	s_cmpk_gt_u32 s33, 0x7cff
	s_cbranch_scc0 .LBB0_728
	s_cmpk_gt_u32 s33, 0x84ff
	s_cbranch_scc0 .LBB0_725
	s_mov_b64 s[60:61], -1
	s_cmp_gt_u32 s33, 0x244ff
	s_mov_b64 s[56:57], -1
	s_cbranch_scc0 .LBB0_723
	s_add_i32 s56, s72, 0xbb00
	s_bfe_u32 s57, s56, 0x6000a
	s_mulk_i32 s57, 0x2493
	s_lshr_b32 s64, s57, 16
	s_mul_i32 s57, s64, 0x1c00
	s_sub_i32 s56, s56, s57
	s_bfe_u32 s75, s56, 0x50001
	s_bfe_u32 s74, s56, 0xa0006
	s_lshl_b32 s74, s74, 1
	s_and_b32 s56, s56, 1
	s_or_b32 s74, s74, s56
	s_mov_b64 s[56:57], 0
